# baseline (speedup 1.0000x reference)
_Z6gat_k1PKfS0_S0_S0_PDF16_S1_S1_Pf:
	s_load_dwordx8 s[4:11], s[0:1], 0x0
	s_load_dwordx8 s[12:19], s[0:1], 0x20
	v_lshrrev_b32_e32 v54, 6, v0
	v_and_b32_e32 v57, 0xc0, v0
	s_lshl_b32 s3, s2, 5
	v_and_b32_e32 v1, 63, v0
	v_bfe_u32 v55, v0, 5, 1
	v_lshlrev_b32_e32 v2, 8, v57
	v_mov_b32_e32 v19, 0
	v_or_b32_e32 v4, s3, v54
	v_and_b32_e32 v56, 31, v0
	v_lshl_or_b32 v18, v55, 11, v2
	v_lshlrev_b32_e32 v20, 4, v1
	v_mov_b32_e32 v21, v19
	v_ashrrev_i32_e32 v5, 31, v4
	s_waitcnt lgkmcnt(0)
	v_lshl_add_u64 v[2:3], s[6:7], 0, v[18:19]
	v_lshlrev_b32_e32 v18, 2, v56
	v_lshl_add_u64 v[6:7], s[4:5], 0, v[20:21]
	v_lshlrev_b64 v[8:9], 10, v[4:5]
	v_lshl_add_u64 v[2:3], v[2:3], 0, v[18:19]
	v_lshl_add_u64 v[10:11], v[6:7], 0, v[8:9]
	v_or_b32_e32 v12, 0x1000, v8
	v_mov_b32_e32 v13, v9
	global_load_dword v58, v[2:3], off
	global_load_dword v59, v[2:3], off offset:128
	global_load_dword v60, v[2:3], off offset:256
	global_load_dword v61, v[2:3], off offset:384
	global_load_dword v62, v[2:3], off offset:512
	global_load_dword v63, v[2:3], off offset:640
	global_load_dword v64, v[2:3], off offset:768
	global_load_dword v65, v[2:3], off offset:896
	v_lshl_add_u64 v[12:13], v[6:7], 0, v[12:13]
	global_load_dwordx4 v[22:25], v[10:11], off nt
	global_load_dwordx4 v[26:29], v[12:13], off nt
	v_or_b32_e32 v10, 0x2000, v8
	v_mov_b32_e32 v11, v9
	v_or_b32_e32 v8, 0x3000, v8
	v_lshl_add_u64 v[10:11], v[6:7], 0, v[10:11]
	v_lshl_add_u64 v[8:9], v[6:7], 0, v[8:9]
	global_load_dwordx4 v[30:33], v[10:11], off nt
	global_load_dwordx4 v[34:37], v[8:9], off nt
	v_or_b32_e32 v8, 16, v4
	v_ashrrev_i32_e32 v9, 31, v8
	v_or_b32_e32 v10, 20, v4
	v_lshlrev_b64 v[8:9], 10, v[8:9]
	v_ashrrev_i32_e32 v11, 31, v10
	v_lshl_add_u64 v[8:9], v[6:7], 0, v[8:9]
	v_lshlrev_b64 v[10:11], 10, v[10:11]
	v_lshl_add_u64 v[10:11], v[6:7], 0, v[10:11]
	global_load_dwordx4 v[38:41], v[8:9], off nt
	global_load_dwordx4 v[42:45], v[10:11], off nt
	v_or_b32_e32 v8, 24, v4
	v_ashrrev_i32_e32 v9, 31, v8
	v_or_b32_e32 v4, 28, v4
	v_lshlrev_b64 v[8:9], 10, v[8:9]
	v_ashrrev_i32_e32 v5, 31, v4
	v_lshl_add_u64 v[8:9], v[6:7], 0, v[8:9]
	v_lshlrev_b64 v[4:5], 10, v[4:5]
	v_lshl_add_u64 v[4:5], v[6:7], 0, v[4:5]
	global_load_dwordx4 v[46:49], v[8:9], off nt
	global_load_dwordx4 v[50:53], v[4:5], off nt
	global_load_dword v19, v[2:3], off offset:1024
	global_load_dword v66, v[2:3], off offset:1152
	global_load_dword v67, v[2:3], off offset:1280
	global_load_dword v68, v[2:3], off offset:1408
	global_load_dword v69, v[2:3], off offset:1536
	global_load_dword v70, v[2:3], off offset:1664
	global_load_dword v71, v[2:3], off offset:1792
	global_load_dword v72, v[2:3], off offset:1920
	s_movk_i32 s4, 0x1000
	v_add_co_u32_e32 v4, vcc, s4, v2
	s_movk_i32 s4, 0x2000
	s_nop 0
	v_addc_co_u32_e32 v5, vcc, 0, v3, vcc
	v_add_co_u32_e32 v6, vcc, s4, v2
	s_movk_i32 s4, 0x3000
	s_nop 0
	v_addc_co_u32_e32 v7, vcc, 0, v3, vcc
	global_load_dword v73, v[4:5], off offset:128
	global_load_dword v74, v[4:5], off offset:256
	global_load_dword v75, v[4:5], off offset:384
	global_load_dword v76, v[4:5], off offset:512
	global_load_dword v77, v[4:5], off offset:640
	global_load_dword v78, v[4:5], off offset:768
	global_load_dword v79, v[4:5], off offset:896
	global_load_dword v80, v[4:5], off offset:1024
	global_load_dword v81, v[4:5], off offset:1152
	global_load_dword v82, v[4:5], off offset:1280
	global_load_dword v83, v[4:5], off offset:1408
	global_load_dword v84, v[4:5], off offset:1536
	global_load_dword v85, v[4:5], off offset:1664
	global_load_dword v86, v[4:5], off offset:1792
	global_load_dword v87, v[4:5], off offset:1920
	global_load_dword v88, v[6:7], off offset:-4096
	global_load_dword v89, v[6:7], off
	global_load_dword v90, v[6:7], off offset:128
	global_load_dword v91, v[6:7], off offset:256
	global_load_dword v92, v[6:7], off offset:384
	global_load_dword v93, v[6:7], off offset:512
	global_load_dword v94, v[6:7], off offset:640
	global_load_dword v95, v[6:7], off offset:768
	global_load_dword v96, v[6:7], off offset:896
	global_load_dword v97, v[6:7], off offset:1024
	global_load_dword v98, v[6:7], off offset:1152
	global_load_dword v99, v[6:7], off offset:1280
	global_load_dword v100, v[6:7], off offset:1408
	global_load_dword v101, v[6:7], off offset:1536
	global_load_dword v102, v[6:7], off offset:1664
	global_load_dword v103, v[6:7], off offset:1792
	global_load_dword v104, v[6:7], off offset:1920
	v_add_co_u32_e32 v2, vcc, s4, v2
	v_and_b32_e32 v1, 7, v0
	s_nop 0
	v_addc_co_u32_e32 v3, vcc, 0, v3, vcc
	global_load_dword v105, v[2:3], off
	global_load_dword v106, v[2:3], off offset:128
	global_load_dword v107, v[2:3], off offset:256
	global_load_dword v108, v[2:3], off offset:384
	global_load_dword v109, v[2:3], off offset:512
	global_load_dword v110, v[2:3], off offset:640
	global_load_dword v111, v[2:3], off offset:768
	global_load_dword v112, v[2:3], off offset:896
	global_load_dword v113, v[2:3], off offset:1024
	global_load_dword v114, v[2:3], off offset:1152
	global_load_dword v115, v[2:3], off offset:1280
	global_load_dword v116, v[2:3], off offset:1408
	global_load_dword v117, v[2:3], off offset:1536
	global_load_dword v118, v[2:3], off offset:1664
	global_load_dword v119, v[2:3], off offset:1792
	global_load_dword v120, v[2:3], off offset:1920
	v_lshlrev_b32_e32 v121, 5, v1
	global_load_dwordx4 v[6:9], v121, s[8:9]
	global_load_dwordx4 v[2:5], v121, s[10:11]
	global_load_dwordx4 v[14:17], v121, s[8:9] offset:16
	global_load_dwordx4 v[10:13], v121, s[10:11] offset:16
	s_movk_i32 s4, 0x410
	v_mad_u32_u24 v122, v54, s4, v20
	s_movk_i32 s8, 0x110
	s_waitcnt vmcnt(62)
	ds_write_b128 v122, v[22:25] offset:34816
	ds_write_b128 v122, v[26:29] offset:38976
	ds_write_b128 v122, v[30:33] offset:43136
	ds_write_b128 v122, v[34:37] offset:47296
	ds_write_b128 v122, v[38:41] offset:51456
	ds_write_b128 v122, v[42:45] offset:55616
	s_waitcnt vmcnt(61)
	ds_write_b128 v122, v[46:49] offset:59776
	s_waitcnt vmcnt(60)
	ds_write_b128 v122, v[50:53] offset:63936
	v_mul_u32_u24_e32 v22, 0x410, v56
	v_lshlrev_b32_e32 v23, 2, v57
	v_and_b32_e32 v24, 32, v0
	v_add3_u32 v38, v22, v23, v24
	s_waitcnt lgkmcnt(0)
	s_barrier
	ds_read_b128 v[22:25], v38 offset:34832
	ds_read_b128 v[26:29], v38 offset:34816
	ds_read_b128 v[30:33], v38 offset:34880
	ds_read_b128 v[34:37], v38 offset:34896
	s_waitcnt lgkmcnt(3)
	v_cvt_pk_f16_f32 v25, v24, v25
	v_cvt_pk_f16_f32 v24, v22, v23
	s_waitcnt lgkmcnt(2)
	v_cvt_pk_f16_f32 v23, v28, v29
	v_cvt_pk_f16_f32 v22, v26, v27
	s_waitcnt vmcnt(53)
	v_cvt_pk_f16_f32 v29, v69, v71
	v_cvt_pk_f16_f32 v28, v19, v67
	v_cvt_pk_f16_f32 v27, v62, v64
	v_cvt_pk_f16_f32 v26, v58, v60
	v_lshlrev_b32_e32 v19, 2, v55
	s_nop 0
	v_mfma_f32_32x32x16_f16 a[0:15], v[22:25], v[26:29], 0
	s_waitcnt vmcnt(52)
	v_cvt_pk_f16_f32 v29, v70, v72
	v_cvt_pk_f16_f32 v28, v66, v68
	v_cvt_pk_f16_f32 v27, v63, v65
	v_cvt_pk_f16_f32 v26, v59, v61
	s_nop 1
	v_mfma_f32_32x32x16_f16 a[16:31], v[22:25], v[26:29], 0
	s_waitcnt lgkmcnt(0)
	v_cvt_pk_f16_f32 v25, v36, v37
	v_cvt_pk_f16_f32 v24, v34, v35
	v_cvt_pk_f16_f32 v23, v32, v33
	v_cvt_pk_f16_f32 v22, v30, v31
	ds_read_b128 v[30:33], v38 offset:34944
	ds_read_b128 v[34:37], v38 offset:34960
	s_waitcnt vmcnt(38)
	v_cvt_pk_f16_f32 v29, v84, v86
	v_cvt_pk_f16_f32 v28, v80, v82
	v_cvt_pk_f16_f32 v27, v76, v78
	s_waitcnt vmcnt(36)
	v_cvt_pk_f16_f32 v26, v88, v74
	s_nop 1
	v_mfma_f32_32x32x16_f16 a[0:15], v[22:25], v[26:29], a[0:15]
	v_cvt_pk_f16_f32 v29, v85, v87
	v_cvt_pk_f16_f32 v28, v81, v83
	v_cvt_pk_f16_f32 v27, v77, v79
	v_cvt_pk_f16_f32 v26, v73, v75
	s_nop 1
	v_mfma_f32_32x32x16_f16 a[16:31], v[22:25], v[26:29], a[16:31]
	s_waitcnt lgkmcnt(0)
	v_cvt_pk_f16_f32 v25, v36, v37
	v_cvt_pk_f16_f32 v24, v34, v35
	v_cvt_pk_f16_f32 v23, v32, v33
	v_cvt_pk_f16_f32 v22, v30, v31
	ds_read_b128 v[30:33], v38 offset:35008
	ds_read_b128 v[34:37], v38 offset:35024
	s_waitcnt vmcnt(21)
	v_cvt_pk_f16_f32 v29, v101, v103
	v_cvt_pk_f16_f32 v28, v97, v99
	v_cvt_pk_f16_f32 v27, v93, v95
	v_cvt_pk_f16_f32 v26, v89, v91
	s_nop 1
	v_mfma_f32_32x32x16_f16 a[0:15], v[22:25], v[26:29], a[0:15]
	s_waitcnt vmcnt(20)
	v_cvt_pk_f16_f32 v29, v102, v104
	v_cvt_pk_f16_f32 v28, v98, v100
	v_cvt_pk_f16_f32 v27, v94, v96
	v_cvt_pk_f16_f32 v26, v90, v92
	s_nop 1
	v_mfma_f32_32x32x16_f16 a[16:31], v[22:25], v[26:29], a[16:31]
	s_waitcnt lgkmcnt(0)
	v_cvt_pk_f16_f32 v25, v36, v37
	v_cvt_pk_f16_f32 v24, v34, v35
	v_cvt_pk_f16_f32 v23, v32, v33
	v_cvt_pk_f16_f32 v22, v30, v31
	s_waitcnt vmcnt(5)
	v_cvt_pk_f16_f32 v29, v117, v119
	v_cvt_pk_f16_f32 v28, v113, v115
	v_cvt_pk_f16_f32 v27, v109, v111
	v_cvt_pk_f16_f32 v26, v105, v107
	s_nop 1
	v_mfma_f32_32x32x16_f16 a[0:15], v[22:25], v[26:29], a[0:15]
	s_waitcnt vmcnt(4)
	v_cvt_pk_f16_f32 v29, v118, v120
	v_cvt_pk_f16_f32 v28, v114, v116
	v_cvt_pk_f16_f32 v27, v110, v112
	v_cvt_pk_f16_f32 v26, v106, v108
	s_nop 1
	v_mfma_f32_32x32x16_f16 a[16:31], v[22:25], v[26:29], a[16:31]
	v_lshl_or_b32 v22, v54, 5, v19
	v_mul_u32_u24_e32 v22, 0x44, v22
	v_lshl_add_u32 v22, v22, 2, v18
	s_nop 0
	ds_write_b32 v22, a0
	s_nop 6
	ds_write_b32 v22, a16 offset:128
	ds_write_b32 v22, a1 offset:272
	ds_write_b32 v22, a17 offset:400
	ds_write_b32 v22, a2 offset:544
	ds_write_b32 v22, a18 offset:672
	ds_write_b32 v22, a3 offset:816
	ds_write_b32 v22, a19 offset:944
	ds_write_b32 v22, a4 offset:2176
	ds_write_b32 v22, a20 offset:2304
	ds_write_b32 v22, a5 offset:2448
	ds_write_b32 v22, a21 offset:2576
	ds_write_b32 v22, a6 offset:2720
	ds_write_b32 v22, a22 offset:2848
	ds_write_b32 v22, a7 offset:2992
	ds_write_b32 v22, a23 offset:3120
	ds_write_b32 v22, a8 offset:4352
	ds_write_b32 v22, a24 offset:4480
	ds_write_b32 v22, a9 offset:4624
	ds_write_b32 v22, a25 offset:4752
	ds_write_b32 v22, a10 offset:4896
	ds_write_b32 v22, a26 offset:5024
	ds_write_b32 v22, a11 offset:5168
	ds_write_b32 v22, a27 offset:5296
	ds_write_b32 v22, a12 offset:6528
	ds_write_b32 v22, a28 offset:6656
	ds_write_b32 v22, a13 offset:6800
	ds_write_b32 v22, a29 offset:6928
	ds_write_b32 v22, a14 offset:7072
	ds_write_b32 v22, a30 offset:7200
	ds_write_b32 v22, a15 offset:7344
	ds_write_b32 v22, a31 offset:7472
	v_lshrrev_b32_e32 v22, 3, v0
	v_mad_u32_u24 v23, v22, s8, v121
	s_waitcnt lgkmcnt(0)
	s_barrier
	ds_read_b128 v[24:27], v23
	ds_read_b128 v[28:31], v23 offset:16
	ds_read_b128 v[32:35], v23 offset:8704
	s_waitcnt lgkmcnt(2)
	v_pk_add_f32 v[36:37], v[26:27], 0 op_sel_hi:[1,0]
	v_pk_add_f32 v[38:39], v[24:25], 0 op_sel_hi:[1,0]
	ds_read_b128 v[24:27], v23 offset:8720
	s_waitcnt lgkmcnt(2)
	v_pk_add_f32 v[40:41], v[30:31], 0 op_sel_hi:[1,0]
	v_pk_add_f32 v[42:43], v[28:29], 0 op_sel_hi:[1,0]
	ds_read_b128 v[28:31], v23 offset:17408
	s_waitcnt lgkmcnt(2)
	v_pk_add_f32 v[34:35], v[36:37], v[34:35]
	v_pk_add_f32 v[36:37], v[38:39], v[32:33]
	s_waitcnt lgkmcnt(1)
	v_pk_add_f32 v[38:39], v[40:41], v[26:27]
	v_pk_add_f32 v[40:41], v[42:43], v[24:25]
	ds_read_b128 v[24:27], v23 offset:17424
	s_waitcnt lgkmcnt(1)
	v_pk_add_f32 v[42:43], v[34:35], v[30:31]
	ds_read_b128 v[30:33], v23 offset:26112
	v_pk_add_f32 v[28:29], v[36:37], v[28:29]
	ds_read_b128 v[34:37], v23 offset:26128
	s_waitcnt lgkmcnt(2)
	v_pk_add_f32 v[40:41], v[40:41], v[24:25]
	v_pk_add_f32 v[38:39], v[38:39], v[26:27]
	s_waitcnt lgkmcnt(1)
	v_pk_add_f32 v[24:25], v[28:29], v[30:31]
	v_pk_add_f32 v[26:27], v[42:43], v[32:33]
	s_waitcnt lgkmcnt(0)
	v_pk_add_f32 v[28:29], v[40:41], v[34:35]
	v_pk_add_f32 v[30:31], v[38:39], v[36:37]
	s_waitcnt vmcnt(0)
	v_mul_f32_e32 v10, v28, v10
	v_fmac_f32_e32 v10, v24, v2
	v_mul_f32_e32 v14, v28, v14
	v_add_f32_e32 v2, 0, v10
	v_mul_f32_e32 v10, v29, v15
	v_fmac_f32_e32 v14, v24, v6
	v_fmac_f32_e32 v10, v25, v7
	v_mul_f32_e32 v7, v29, v11
	v_add_f32_e32 v6, 0, v14
	v_fmac_f32_e32 v7, v25, v3
	v_mul_f32_e32 v3, v30, v16
	v_add_f32_e32 v6, v6, v10
	v_fmac_f32_e32 v3, v26, v8
	v_add_f32_e32 v3, v6, v3
	v_mul_f32_e32 v6, v30, v12
	v_fmac_f32_e32 v6, v26, v4
	v_mul_f32_e32 v4, v31, v17
	v_fmac_f32_e32 v4, v27, v9
	v_add_f32_e32 v2, v2, v7
	v_add_f32_e32 v3, v3, v4
	v_mul_f32_e32 v4, v31, v13
	v_add_f32_e32 v2, v2, v6
	v_fmac_f32_e32 v4, v27, v5
	v_add_f32_e32 v2, v2, v4
	ds_write_b128 v23, v[24:27]
	ds_write_b128 v23, v[28:31] offset:16
	s_nop 1
	v_add_f32_dpp v3, v3, v3 quad_perm:[1,0,3,2] row_mask:0xf bank_mask:0xf
	v_add_f32_dpp v6, v2, v2 quad_perm:[1,0,3,2] row_mask:0xf bank_mask:0xf
	s_nop 1
	v_add_f32_dpp v3, v3, v3 quad_perm:[2,3,0,1] row_mask:0xf bank_mask:0xf
	v_add_f32_dpp v6, v6, v6 quad_perm:[2,3,0,1] row_mask:0xf bank_mask:0xf
	s_nop 1
	v_add_f32_dpp v2, v3, v3 row_half_mirror row_mask:0xf bank_mask:0xf
	v_add_f32_dpp v3, v6, v6 row_half_mirror row_mask:0xf bank_mask:0xf
	v_cmp_eq_u32_e32 vcc, 0, v1
	s_and_saveexec_b64 s[6:7], vcc
	s_cbranch_execz .LBB0_2
	v_mul_f32_e32 v4, 0x3f7d70a4, v3
	v_mul_f32_e32 v4, 0x3fb8aa3b, v4
	v_mul_f32_e32 v3, 0x3c23d70a, v3
	v_exp_f32_e32 v4, v4
	v_mul_f32_e32 v3, 0x3fb8aa3b, v3
	v_exp_f32_e32 v3, v3
	v_lshlrev_b32_e32 v5, 2, v22
	v_or_b32_e32 v6, 0x10a80, v5
	v_mul_f32_e32 v2, 0xbf7d70a4, v2
	ds_write_b32 v6, v4
	v_or_b32_e32 v4, 0x10a00, v5
	v_mul_f32_e32 v2, 0x3fb8aa3b, v2
	ds_write_b32 v4, v3
	v_exp_f32_e32 v4, v2
	v_add_u32_e32 v2, s3, v22
	v_ashrrev_i32_e32 v3, 31, v2
	v_lshl_add_u64 v[2:3], v[2:3], 2, s[18:19]
	global_store_dword v[2:3], v4, off sc1
.LBB0_2:
	s_or_b64 exec, exec, s[6:7]
	v_bfe_u32 v16, v0, 6, 1
	v_lshl_or_b32 v2, v16, 4, v19
	s_movk_i32 s6, 0x80
	v_and_or_b32 v3, v0, s6, v18
	v_lshlrev_b32_e32 v6, 2, v2
	v_mad_u32_u24 v12, v2, s8, v3
	v_or_b32_e32 v2, 0x10a00, v6
	v_or_b32_e32 v6, 0x10a20, v6
	v_add_u32_e32 v14, 0x800, v12
	v_lshlrev_b32_e32 v50, 2, v0
	v_and_b32_e32 v50, 0x200, v50
	v_lshl_add_u32 v50, s2, 1, v50
	v_or_b32_e32 v50, v50, v16
	v_ashrrev_i32_e32 v51, 31, v50
	v_lshlrev_b64 v[50:51], 10, v[50:51]
	v_lshl_add_u64 v[50:51], s[12:13], 0, v[50:51]
	v_lshl_add_u64 v[50:51], v[50:51], 0, v[20:21]
	v_lshlrev_b32_e32 v40, 1, v0
	v_bfe_u32 v41, v0, 3, 1
	v_and_b32_e32 v40, 8, v40
	v_and_b32_e32 v42, 16, v0
	v_and_or_b32 v43, v0, 3, v40
	v_lshlrev_b32_e32 v40, 2, v41
	v_or3_b32 v43, v43, v40, v42
	v_lshlrev_b32_e32 v43, 2, v43
	v_or_b32_e32 v44, 0x10a80, v43
	v_or_b32_e32 v45, 0x10a00, v43
	v_lshl_or_b32 v46, v41, 3, s3
	v_or3_b32 v46, v46, v42, v1
	v_ashrrev_i32_e32 v47, 31, v46
	v_lshlrev_b64 v[46:47], 1, v[46:47]
	v_lshl_add_u64 v[48:49], s[14:15], 0, v[46:47]
	v_lshl_add_u64 v[46:47], s[16:17], 0, v[46:47]
	v_cmp_gt_u32_e32 vcc, 32, v0
	s_waitcnt lgkmcnt(0)
	s_barrier
	ds_read2_b32 v[10:11], v12 offset1:68
	ds_read_b128 v[2:5], v2
	ds_read_b128 v[6:9], v6
	ds_read2_b32 v[52:53], v12 offset0:136 offset1:204
	ds_read2_b32 v[12:13], v14 offset0:32 offset1:100
	ds_read2_b32 v[14:15], v14 offset0:168 offset1:236
	ds_read_b32 v44, v44
	ds_read_b32 v45, v45
	s_waitcnt lgkmcnt(6)
	v_pk_mul_f32 v[2:3], v[10:11], v[2:3]
	s_waitcnt lgkmcnt(4)
	v_pk_mul_f32 v[4:5], v[52:53], v[4:5]
	v_cvt_pk_f16_f32 v2, v2, v3
	v_cvt_pk_f16_f32 v3, v4, v5
	s_waitcnt lgkmcnt(3)
	v_pk_mul_f32 v[4:5], v[12:13], v[6:7]
	s_waitcnt lgkmcnt(2)
	v_pk_mul_f32 v[6:7], v[14:15], v[8:9]
	v_cvt_pk_f16_f32 v4, v4, v5
	v_cvt_pk_f16_f32 v5, v6, v7
	global_store_dwordx4 v[50:51], v[2:5], off sc1
	s_and_saveexec_b64 s[4:5], vcc
	s_cbranch_execz .LBB0_4
	s_waitcnt lgkmcnt(0)
	v_cvt_f16_f32_e32 v44, v44
	v_cvt_f16_f32_e32 v45, v45
	global_store_short v[48:49], v44, off sc1
	global_store_short v[46:47], v45, off sc1
